# speedup vs baseline: 1.0406x; 1.0220x over previous
.LBB5_150:
	s_lshl_b32 s10, s33, 8
	s_add_u32 s16, s34, s10
	s_addc_u32 s17, s35, 0
	v_mov_b32_e32 v83, 0
	v_lshl_add_u64 v[0:1], s[16:17], 0, v[82:83]
	s_mov_b64 s[16:17], 0x151000
	v_cmp_gt_u32_e64 s[10:11], 31, v128
	v_cmp_lt_u32_e64 s[12:13], 30, v128
	v_lshl_add_u64 v[0:1], v[0:1], 0, s[16:17]
	v_mov_b64_e32 v[2:3], 0
	s_mov_b32 s24, 0x400001
	s_mov_b64 s[16:17], 0xffffffff
	s_sleep 16
	s_branch .LBB5_152

.LBB5_184:
	s_lshl_b32 s2, s33, 8
	s_add_u32 s8, s34, s2
	s_addc_u32 s9, s35, 0
	v_mov_b32_e32 v83, 0
	s_waitcnt vmcnt(7)
	v_lshl_add_u64 v[36:37], s[8:9], 0, v[82:83]
	s_mov_b64 s[8:9], 0x151800
	v_cmp_gt_u32_e64 s[2:3], 31, v128
	v_cmp_lt_u32_e64 s[4:5], 30, v128
	v_lshl_add_u64 v[36:37], v[36:37], 0, s[8:9]
	s_waitcnt vmcnt(6)
	v_mov_b64_e32 v[38:39], 0
	s_mov_b32 s12, 0x400001
	s_mov_b64 s[8:9], 0xffffffff
	s_sleep 16
	s_branch .LBB5_186
